# v1 + alignment padding restoring the original 64B phase of all code after the indexer
# speedup vs baseline: 1.0064x; 1.0064x over previous
.LBB0_1251:
	s_andn2_b64 vcc, exec, s[24:25]
	s_cbranch_vccnz .LBB0_1151
	s_cmpk_gt_i32 s13, 0xff
	s_mov_b64 s[2:3], -1
	s_cbranch_scc0 .LBB0_1852
	s_cmp_gt_i32 s14, 4
	s_cselect_b64 s[28:29], -1, 0
	s_cmp_gt_i32 s14, 8
	s_cselect_b64 s[26:27], -1, 0
	s_cmp_gt_i32 s14, 12
	s_cselect_b64 s[2:3], -1, 0
	s_waitcnt vmcnt(0)
	v_mov_b32_e32 v67, 15
	v_mov_b32_e32 v66, 0
	s_branch .LBB0_1255
	s_nop 0
	s_nop 0
	s_nop 0
	s_nop 0
	s_nop 0

.LBB0_1961:
	s_or_b64 exec, exec, s[10:11]
	s_mov_b64 s[10:11], exec
	v_mbcnt_lo_u32_b32 v2, s10, 0
	v_mbcnt_hi_u32_b32 v2, s11, v2
	v_cmp_eq_u32_e32 vcc, 0, v2
	s_waitcnt vmcnt(0)
	buffer_inv sc1
	s_and_saveexec_b64 s[12:13], vcc
	s_cbranch_execz .LBB0_1910
	s_bcnt1_i32_b64 s10, s[10:11]
	v_mov_b32_e32 v2, s10
	global_atomic_add v1, v2, s[68:69]
	s_branch .LBB0_1910
	s_nop 0
	s_nop 0
	s_nop 0
	s_nop 0
	s_nop 0
	s_nop 0
